# P4 out-proj epilogue: 16-byte residual loads and output stores issued with a lane permutation (ds_bpermute) so each quad of lanes covers 64 contiguous bytes
# speedup vs baseline: 1.0046x; 1.0046x over previous
; #define GAS __attribute__((address_space(1)))
; __device__ __forceinline__ float bflo(unsigned w) { return __uint_as_float(w << 16); }
; __device__ __forceinline__ float bfhi(unsigned w) { return __uint_as_float(w & 0xffff0000u); }
; __device__ __forceinline__ u32x4 pack8(const f32x4& a, const f32x4& b) { u32x4 w; w.x = cvt_pk_bf16(a[0], a[1]); w.y = cvt_pk_bf16(a[2], a[3]); w.z = cvt_pk_bf16(b[0], b[1]); w.w = cvt_pk_bf16(b[2], b[3]); return w; }
; __device__ __forceinline__ float sum4sq(const f32x4& a) { return (a[0] * a[0] + a[1] * a[1]) + (a[2] * a[2] + a[3] * a[3]); }
;     __device__ __forceinline__ void operator()(const AccT& acc, const Unit& u, int wr, int wc, int fr, int fq, const LAS f32x2* tab) const {
;     ...
;         for (int ai = 0; ai < 2; ++ai) {
;             u32x4 xwv[4][2];
; _Pragma("unroll")
;             for (int m = 0; m < 4; ++m)
; _Pragma("unroll")
;                 for (int bj = 0; bj < 2; ++bj) xwv[m][bj] = *(const GAS u32x4*)(xag + (size_t)(u.pm * 256 + ai * 128 + wr * 64 + m * 16 + fr) * 1024 + u.pn * 256 + bj * 128 + wc * 32 + fq * 8);
;             asm volatile("" ::: "memory");
; _Pragma("unroll")
;             for (int m = 0; m < 4; ++m) { const int rl = ai * 128 + wr * 64 + m * 16 + fr; const int row = u.pm * 256 + rl; const float rf = tab[rl].y; float s = 0.f;
; _Pragma("unroll")
;                 for (int bj = 0; bj < 2; ++bj) { const size_t off = (size_t)row * 1024 + u.pn * 256 + bj * 128 + wc * 32 + fq * 8; f32x4 b0, b1;
;                     { const u32x4 w = xwv[m][bj]; b0 = (f32x4){bflo(w.x), bfhi(w.x), bflo(w.y), bfhi(w.y)}; b1 = (f32x4){bflo(w.z), bfhi(w.z), bflo(w.w), bfhi(w.w)}; }
;                     const f32x4 v0 = b0 + acc[ai][bj][m][0] * rf, v1 = b1 + acc[ai][bj][m][1] * rf; s += sum4sq(v0) + sum4sq(v1);
;                     *(u32x4*)(xb + off) = pack8(v0, v1); }
;                 s = red_fq(s); if (fq == 0) ssx1[(size_t)row * 16 + u.pn * 4 + wc] = s; }
.LBB0_1627:
	v_mbcnt_lo_u32_b32 v220, -1, 0
	v_mbcnt_hi_u32_b32 v220, -1, v220
	v_lshrrev_b32_e32 v221, 4, v220
	v_and_b32_e32 v232, 3, v220
	v_and_or_b32 v221, v220, 12, v221
	v_lshl_or_b32 v220, v232, 4, v221
	v_lshlrev_b32_e32 v220, 2, v220
	s_lshl_b32 s26, s85, 11
	s_and_b32 s26, s26, 0x800
	s_add_i32 s42, s52, s26
	v_mov_b32_e32 v130, v184
	v_mov_b32_e32 v132, v134
	s_lshl_b32 s26, s79, 8
	s_ashr_i32 s27, s26, 31
	v_add_u32_e32 v204, s68, v132
	s_lshl_b64 s[26:27], s[26:27], 1
	v_lshlrev_b32_e32 v132, 3, v130
	v_lshl_add_u32 v170, s84, 8, v204
	s_add_u32 s40, s70, s26
	v_ashrrev_i32_e32 v133, 31, v132
	s_addc_u32 s41, s71, s27
	v_lshlrev_b64 v[132:133], 1, v[132:133]
	v_ashrrev_i32_e32 v171, 31, v170
	v_lshl_add_u64 v[168:169], s[40:41], 0, v[132:133]
	v_lshlrev_b64 v[200:201], 11, v[170:171]
	v_lshl_add_u64 v[142:143], v[168:169], 0, v[200:201]
	ds_bpermute_b32 v214, v220, v142
	ds_bpermute_b32 v215, v220, v143
	s_waitcnt lgkmcnt(0)
	global_load_dwordx4 v[192:195], v[214:215], off
	global_load_dwordx4 v[196:199], v[214:215], off offset:256
	v_add_u32_e32 v178, 16, v170
	v_add_u32_e32 v174, 32, v170
	v_add_u32_e32 v172, 48, v170
	v_ashrrev_i32_e32 v179, 31, v178
	v_ashrrev_i32_e32 v175, 31, v174
	v_ashrrev_i32_e32 v173, 31, v172
	v_lshlrev_b64 v[182:183], 11, v[178:179]
	v_lshlrev_b64 v[180:181], 11, v[174:175]
	v_lshlrev_b64 v[176:177], 11, v[172:173]
	v_lshl_add_u64 v[142:143], v[168:169], 0, v[182:183]
	v_lshl_add_u64 v[144:145], v[168:169], 0, v[180:181]
	v_lshl_add_u64 v[202:203], v[168:169], 0, v[176:177]
	ds_bpermute_b32 v214, v220, v142
	ds_bpermute_b32 v215, v220, v143
	s_waitcnt lgkmcnt(0)
	global_load_dwordx4 v[162:165], v[214:215], off
	global_load_dwordx4 v[158:161], v[214:215], off offset:256
	ds_bpermute_b32 v214, v220, v144
	ds_bpermute_b32 v215, v220, v145
	s_waitcnt lgkmcnt(0)
	global_load_dwordx4 v[154:157], v[214:215], off
	global_load_dwordx4 v[150:153], v[214:215], off offset:256
	ds_bpermute_b32 v214, v220, v202
	ds_bpermute_b32 v215, v220, v203
	s_waitcnt lgkmcnt(0)
	global_load_dwordx4 v[146:149], v[214:215], off
	s_nop 0
	global_load_dwordx4 v[142:145], v[214:215], off offset:256
	v_cmp_eq_u32_e32 vcc, 0, v130
	v_lshl_add_u32 v130, v204, 3, s42
	s_waitcnt vmcnt(0)
	ds_bpermute_b32 v192, v220, v192
	ds_bpermute_b32 v193, v220, v193
	ds_bpermute_b32 v194, v220, v194
	ds_bpermute_b32 v195, v220, v195
	ds_bpermute_b32 v196, v220, v196
	ds_bpermute_b32 v197, v220, v197
	ds_bpermute_b32 v198, v220, v198
	ds_bpermute_b32 v199, v220, v199
	ds_bpermute_b32 v162, v220, v162
	ds_bpermute_b32 v163, v220, v163
	ds_bpermute_b32 v164, v220, v164
	ds_bpermute_b32 v165, v220, v165
	ds_bpermute_b32 v158, v220, v158
	ds_bpermute_b32 v159, v220, v159
	ds_bpermute_b32 v160, v220, v160
	ds_bpermute_b32 v161, v220, v161
	ds_bpermute_b32 v154, v220, v154
	ds_bpermute_b32 v155, v220, v155
	ds_bpermute_b32 v156, v220, v156
	ds_bpermute_b32 v157, v220, v157
	ds_bpermute_b32 v150, v220, v150
	ds_bpermute_b32 v151, v220, v151
	ds_bpermute_b32 v152, v220, v152
	ds_bpermute_b32 v153, v220, v153
	ds_bpermute_b32 v146, v220, v146
	ds_bpermute_b32 v147, v220, v147
	ds_bpermute_b32 v148, v220, v148
	ds_bpermute_b32 v149, v220, v149
	ds_bpermute_b32 v142, v220, v142
	ds_bpermute_b32 v143, v220, v143
	ds_bpermute_b32 v144, v220, v144
	ds_bpermute_b32 v145, v220, v145
	s_waitcnt lgkmcnt(0)
	ds_read_b64 v[202:203], v130
	s_add_u32 s26, s72, s26
	s_addc_u32 s27, s73, s27
	v_lshl_add_u64 v[132:133], s[26:27], 0, v[132:133]
	v_lshl_add_u64 v[200:201], v[132:133], 0, v[200:201]
	s_lshl_b32 s40, s79, 2
	s_ashr_i32 s41, s40, 31
	s_lshl_b64 s[26:27], s[40:41], 2
	s_add_u32 s26, s74, s26
	s_addc_u32 s27, s75, s27
	v_lshlrev_b32_e32 v204, 16, v192
	v_and_b32_e32 v205, 0xffff0000, v192
	v_lshlrev_b32_e32 v192, 16, v193
	v_and_b32_e32 v193, 0xffff0000, v193
	v_lshlrev_b32_e32 v206, 16, v194
	v_and_b32_e32 v207, 0xffff0000, v194
	v_lshlrev_b32_e32 v194, 16, v195
	v_and_b32_e32 v195, 0xffff0000, v195
	v_lshlrev_b32_e32 v208, 16, v196
	v_and_b32_e32 v209, 0xffff0000, v196
	v_lshlrev_b32_e32 v196, 16, v197
	v_and_b32_e32 v197, 0xffff0000, v197
	s_waitcnt lgkmcnt(0)
	v_pk_fma_f32 v[192:193], v[118:119], v[202:203], v[192:193] op_sel:[0,1,0]
	v_pk_fma_f32 v[204:205], v[116:117], v[202:203], v[204:205] op_sel:[0,1,0]
	v_pk_fma_f32 v[122:123], v[122:123], v[202:203], v[194:195] op_sel:[0,1,0]
	v_pk_fma_f32 v[120:121], v[120:121], v[202:203], v[206:207] op_sel:[0,1,0]
	v_pk_fma_f32 v[140:141], v[140:141], v[202:203], v[196:197] op_sel:[0,1,0]
	v_mul_f32_e32 v194, v205, v205
	v_mul_f32_e32 v195, v193, v193
	v_mul_f32_e32 v196, v121, v121
	v_mul_f32_e32 v197, v123, v123
	v_cvt_pk_bf16_f32 v116, v204, v205
	v_cvt_pk_bf16_f32 v117, v192, v193
	v_fmac_f32_e32 v194, v204, v204
	v_fmac_f32_e32 v195, v192, v192
	v_fmac_f32_e32 v196, v120, v120
	v_fmac_f32_e32 v197, v122, v122
	v_pk_fma_f32 v[138:139], v[138:139], v[202:203], v[208:209] op_sel:[0,1,0]
	v_cvt_pk_bf16_f32 v118, v120, v121
	v_cvt_pk_bf16_f32 v119, v122, v123
	ds_bpermute_b32 v216, v220, v116
	ds_bpermute_b32 v217, v220, v117
	ds_bpermute_b32 v218, v220, v118
	ds_bpermute_b32 v219, v220, v119
	ds_bpermute_b32 v212, v220, v200
	ds_bpermute_b32 v213, v220, v201
	s_waitcnt lgkmcnt(0)
	global_store_dwordx4 v[212:213], v[216:219], off
	v_lshlrev_b32_e32 v210, 16, v198
	v_and_b32_e32 v211, 0xffff0000, v198
	v_add_f32_e32 v116, v194, v195
	v_add_f32_e32 v117, v196, v197
	v_lshlrev_b32_e32 v198, 16, v199
	v_and_b32_e32 v199, 0xffff0000, v199
	v_add_f32_e32 v116, v116, v117
	v_mul_f32_e32 v117, v139, v139
	v_mul_f32_e32 v118, v141, v141
	v_pk_fma_f32 v[126:127], v[126:127], v[202:203], v[198:199] op_sel:[0,1,0]
	v_pk_fma_f32 v[124:125], v[124:125], v[202:203], v[210:211] op_sel:[0,1,0]
	v_fmac_f32_e32 v117, v138, v138
	v_fmac_f32_e32 v118, v140, v140
	v_add_f32_e32 v117, v117, v118
	v_mul_f32_e32 v118, v125, v125
	v_mul_f32_e32 v119, v127, v127
	v_fmac_f32_e32 v118, v124, v124
	v_fmac_f32_e32 v119, v126, v126
	v_add_f32_e32 v118, v118, v119
	v_add_f32_e32 v117, v117, v118
	v_add_f32_e32 v120, v116, v117
	v_cvt_pk_bf16_f32 v116, v138, v139
	v_cvt_pk_bf16_f32 v117, v140, v141
	v_cvt_pk_bf16_f32 v118, v124, v125
	v_cvt_pk_bf16_f32 v119, v126, v127
	ds_bpermute_b32 v228, v220, v116
	ds_bpermute_b32 v229, v220, v117
	ds_bpermute_b32 v230, v220, v118
	ds_bpermute_b32 v231, v220, v119
	s_waitcnt lgkmcnt(0)
	global_store_dwordx4 v[212:213], v[228:231], off offset:256
	s_nop 1
	v_mov_b32_e32 v116, v120
	s_nop 1
	v_permlane16_swap_b32_e32 v120, v116
	v_add_f32_e32 v116, v120, v116
	v_mov_b32_e32 v117, v116
	s_nop 1
	v_permlane32_swap_b32_e32 v116, v117
	s_and_saveexec_b64 s[40:41], vcc
	s_cbranch_execz .LBB0_1629
	v_lshlrev_b64 v[118:119], 6, v[170:171]
	v_lshl_add_u64 v[118:119], s[26:27], 0, v[118:119]
	v_add_f32_e32 v116, v116, v117
	global_store_dword v[118:119], v116, off
; __device__ __forceinline__ float bflo(unsigned w) { return __uint_as_float(w << 16); }
; __device__ __forceinline__ float bfhi(unsigned w) { return __uint_as_float(w & 0xffff0000u); }
; __device__ __forceinline__ u32x4 pack8(const f32x4& a, const f32x4& b) { u32x4 w; w.x = cvt_pk_bf16(a[0], a[1]); w.y = cvt_pk_bf16(a[2], a[3]); w.z = cvt_pk_bf16(b[0], b[1]); w.w = cvt_pk_bf16(b[2], b[3]); return w; }
; __device__ __forceinline__ float sum4sq(const f32x4& a) { return (a[0] * a[0] + a[1] * a[1]) + (a[2] * a[2] + a[3] * a[3]); }
;     __device__ __forceinline__ void operator()(const AccT& acc, const Unit& u, int wr, int wc, int fr, int fq, const LAS f32x2* tab) const {
;     ...
;             for (int m = 0; m < 4; ++m) { const int rl = ai * 128 + wr * 64 + m * 16 + fr; const int row = u.pm * 256 + rl; const float rf = tab[rl].y; float s = 0.f;
; _Pragma("unroll")
;                 for (int bj = 0; bj < 2; ++bj) { const size_t off = (size_t)row * 1024 + u.pn * 256 + bj * 128 + wc * 32 + fq * 8; f32x4 b0, b1;
;                     { const u32x4 w = xwv[m][bj]; b0 = (f32x4){bflo(w.x), bfhi(w.x), bflo(w.y), bfhi(w.y)}; b1 = (f32x4){bflo(w.z), bfhi(w.z), bflo(w.w), bfhi(w.w)}; }
;                     const f32x4 v0 = b0 + acc[ai][bj][m][0] * rf, v1 = b1 + acc[ai][bj][m][1] * rf; s += sum4sq(v0) + sum4sq(v1);
;                     *(u32x4*)(xb + off) = pack8(v0, v1); }
;                 s = red_fq(s); if (fq == 0) ssx1[(size_t)row * 16 + u.pn * 4 + wc] = s; }
.LBB0_1629:
	s_or_b64 exec, exec, s[40:41]
	ds_read_b64 v[116:117], v130 offset:128
	v_lshlrev_b32_e32 v120, 16, v162
	v_and_b32_e32 v121, 0xffff0000, v162
	v_lshlrev_b32_e32 v122, 16, v163
	v_and_b32_e32 v123, 0xffff0000, v163
	v_lshlrev_b32_e32 v124, 16, v164
	v_and_b32_e32 v125, 0xffff0000, v164
	v_lshlrev_b32_e32 v126, 16, v165
	v_and_b32_e32 v127, 0xffff0000, v165
	s_waitcnt lgkmcnt(0)
	v_pk_fma_f32 v[114:115], v[114:115], v[116:117], v[122:123] op_sel:[0,1,0]
	v_pk_fma_f32 v[112:113], v[112:113], v[116:117], v[120:121] op_sel:[0,1,0]
	v_pk_fma_f32 v[120:121], v[110:111], v[116:117], v[126:127] op_sel:[0,1,0]
	v_pk_fma_f32 v[110:111], v[108:109], v[116:117], v[124:125] op_sel:[0,1,0]
	v_mul_f32_e32 v108, v113, v113
	v_mul_f32_e32 v109, v115, v115
	v_fmac_f32_e32 v108, v112, v112
	v_fmac_f32_e32 v109, v114, v114
	v_add_f32_e32 v108, v108, v109
	v_mul_f32_e32 v109, v111, v111
	v_mul_f32_e32 v122, v121, v121
	v_fmac_f32_e32 v109, v110, v110
	v_fmac_f32_e32 v122, v120, v120
	v_add_f32_e32 v109, v109, v122
	v_lshl_add_u64 v[118:119], v[132:133], 0, v[182:183]
	v_add_f32_e32 v122, v108, v109
	v_cvt_pk_bf16_f32 v108, v112, v113
	v_cvt_pk_bf16_f32 v109, v114, v115
	v_cvt_pk_bf16_f32 v110, v110, v111
	v_cvt_pk_bf16_f32 v111, v120, v121
	ds_bpermute_b32 v216, v220, v108
	ds_bpermute_b32 v217, v220, v109
	ds_bpermute_b32 v218, v220, v110
	ds_bpermute_b32 v219, v220, v111
	ds_bpermute_b32 v212, v220, v118
	ds_bpermute_b32 v213, v220, v119
	s_waitcnt lgkmcnt(0)
	global_store_dwordx4 v[212:213], v[216:219], off
	v_lshlrev_b32_e32 v112, 16, v160
	v_and_b32_e32 v113, 0xffff0000, v160
	v_lshlrev_b32_e32 v108, 16, v158
	v_and_b32_e32 v109, 0xffff0000, v158
	v_lshlrev_b32_e32 v110, 16, v159
	v_and_b32_e32 v111, 0xffff0000, v159
	v_lshlrev_b32_e32 v114, 16, v161
	v_and_b32_e32 v115, 0xffff0000, v161
	v_pk_fma_f32 v[106:107], v[106:107], v[116:117], v[110:111] op_sel:[0,1,0]
	v_pk_fma_f32 v[104:105], v[104:105], v[116:117], v[108:109] op_sel:[0,1,0]
	v_pk_fma_f32 v[108:109], v[102:103], v[116:117], v[114:115] op_sel:[0,1,0]
	v_pk_fma_f32 v[102:103], v[100:101], v[116:117], v[112:113] op_sel:[0,1,0]
	v_mul_f32_e32 v100, v105, v105
	v_mul_f32_e32 v101, v107, v107
	v_fmac_f32_e32 v100, v104, v104
	v_fmac_f32_e32 v101, v106, v106
	v_add_f32_e32 v100, v100, v101
	v_mul_f32_e32 v101, v103, v103
	v_mul_f32_e32 v110, v109, v109
	v_fmac_f32_e32 v101, v102, v102
	v_fmac_f32_e32 v110, v108, v108
	v_add_f32_e32 v101, v101, v110
	v_add_f32_e32 v100, v100, v101
	v_add_f32_e32 v110, v122, v100
	v_cvt_pk_bf16_f32 v100, v104, v105
	v_cvt_pk_bf16_f32 v101, v106, v107
	v_cvt_pk_bf16_f32 v102, v102, v103
	v_cvt_pk_bf16_f32 v103, v108, v109
	ds_bpermute_b32 v228, v220, v100
	ds_bpermute_b32 v229, v220, v101
	ds_bpermute_b32 v230, v220, v102
	ds_bpermute_b32 v231, v220, v103
	s_waitcnt lgkmcnt(0)
	global_store_dwordx4 v[212:213], v[228:231], off offset:256
	s_nop 1
	v_mov_b32_e32 v100, v110
	s_nop 1
	v_permlane16_swap_b32_e32 v110, v100
	v_add_f32_e32 v100, v110, v100
	v_mov_b32_e32 v101, v100
	s_nop 1
	v_permlane32_swap_b32_e32 v100, v101
	s_and_saveexec_b64 s[40:41], vcc
	s_cbranch_execz .LBB0_1631
	v_lshlrev_b64 v[102:103], 6, v[178:179]
	v_lshl_add_u64 v[102:103], s[26:27], 0, v[102:103]
	v_add_f32_e32 v100, v100, v101
	global_store_dword v[102:103], v100, off
.LBB0_1631:
	s_or_b64 exec, exec, s[40:41]
	ds_read_b64 v[100:101], v130 offset:256
	v_lshlrev_b32_e32 v104, 16, v154
	v_and_b32_e32 v105, 0xffff0000, v154
	v_lshlrev_b32_e32 v106, 16, v155
	v_and_b32_e32 v107, 0xffff0000, v155
	v_lshlrev_b32_e32 v108, 16, v156
	v_and_b32_e32 v109, 0xffff0000, v156
	v_lshlrev_b32_e32 v110, 16, v157
	v_and_b32_e32 v111, 0xffff0000, v157
	s_waitcnt lgkmcnt(0)
	v_pk_fma_f32 v[98:99], v[98:99], v[100:101], v[106:107] op_sel:[0,1,0]
	v_pk_fma_f32 v[96:97], v[96:97], v[100:101], v[104:105] op_sel:[0,1,0]
	v_pk_fma_f32 v[104:105], v[94:95], v[100:101], v[110:111] op_sel:[0,1,0]
	v_pk_fma_f32 v[94:95], v[92:93], v[100:101], v[108:109] op_sel:[0,1,0]
	v_mul_f32_e32 v92, v97, v97
	v_mul_f32_e32 v93, v99, v99
	v_fmac_f32_e32 v92, v96, v96
	v_fmac_f32_e32 v93, v98, v98
	v_add_f32_e32 v92, v92, v93
	v_mul_f32_e32 v93, v95, v95
	v_mul_f32_e32 v106, v105, v105
	v_fmac_f32_e32 v93, v94, v94
	v_fmac_f32_e32 v106, v104, v104
	v_add_f32_e32 v93, v93, v106
	v_lshl_add_u64 v[102:103], v[132:133], 0, v[180:181]
	v_add_f32_e32 v106, v92, v93
	v_cvt_pk_bf16_f32 v92, v96, v97
	v_cvt_pk_bf16_f32 v93, v98, v99
	v_cvt_pk_bf16_f32 v94, v94, v95
	v_cvt_pk_bf16_f32 v95, v104, v105
	ds_bpermute_b32 v216, v220, v92
	ds_bpermute_b32 v217, v220, v93
	ds_bpermute_b32 v218, v220, v94
	ds_bpermute_b32 v219, v220, v95
	ds_bpermute_b32 v212, v220, v102
	ds_bpermute_b32 v213, v220, v103
	s_waitcnt lgkmcnt(0)
	global_store_dwordx4 v[212:213], v[216:219], off
	v_lshlrev_b32_e32 v96, 16, v152
	v_and_b32_e32 v97, 0xffff0000, v152
	v_lshlrev_b32_e32 v92, 16, v150
	v_and_b32_e32 v93, 0xffff0000, v150
	v_lshlrev_b32_e32 v94, 16, v151
	v_and_b32_e32 v95, 0xffff0000, v151
	v_lshlrev_b32_e32 v98, 16, v153
	v_and_b32_e32 v99, 0xffff0000, v153
	v_pk_fma_f32 v[90:91], v[90:91], v[100:101], v[94:95] op_sel:[0,1,0]
	v_pk_fma_f32 v[88:89], v[88:89], v[100:101], v[92:93] op_sel:[0,1,0]
	v_pk_fma_f32 v[92:93], v[86:87], v[100:101], v[98:99] op_sel:[0,1,0]
	v_pk_fma_f32 v[86:87], v[84:85], v[100:101], v[96:97] op_sel:[0,1,0]
	v_mul_f32_e32 v84, v89, v89
	v_mul_f32_e32 v85, v91, v91
	v_fmac_f32_e32 v84, v88, v88
	v_fmac_f32_e32 v85, v90, v90
	v_add_f32_e32 v84, v84, v85
	v_mul_f32_e32 v85, v87, v87
	v_mul_f32_e32 v94, v93, v93
	v_fmac_f32_e32 v85, v86, v86
	v_fmac_f32_e32 v94, v92, v92
	v_add_f32_e32 v85, v85, v94
	v_add_f32_e32 v84, v84, v85
	v_add_f32_e32 v94, v106, v84
	v_cvt_pk_bf16_f32 v84, v88, v89
	v_cvt_pk_bf16_f32 v85, v90, v91
	v_cvt_pk_bf16_f32 v86, v86, v87
	v_cvt_pk_bf16_f32 v87, v92, v93
	ds_bpermute_b32 v228, v220, v84
	ds_bpermute_b32 v229, v220, v85
	ds_bpermute_b32 v230, v220, v86
	ds_bpermute_b32 v231, v220, v87
	s_waitcnt lgkmcnt(0)
	global_store_dwordx4 v[212:213], v[228:231], off offset:256
	s_nop 1
	v_mov_b32_e32 v84, v94
	s_nop 1
	v_permlane16_swap_b32_e32 v94, v84
	v_add_f32_e32 v84, v94, v84
	v_mov_b32_e32 v85, v84
	s_nop 1
	v_permlane32_swap_b32_e32 v84, v85
	s_and_saveexec_b64 s[40:41], vcc
	s_cbranch_execz .LBB0_1633
	v_lshlrev_b64 v[86:87], 6, v[174:175]
	v_lshl_add_u64 v[86:87], s[26:27], 0, v[86:87]
	v_add_f32_e32 v84, v84, v85
	global_store_dword v[86:87], v84, off
; #define GAS __attribute__((address_space(1)))
; __device__ __forceinline__ float bflo(unsigned w) { return __uint_as_float(w << 16); }
; __device__ __forceinline__ float bfhi(unsigned w) { return __uint_as_float(w & 0xffff0000u); }
; __device__ __forceinline__ u32x4 pack8(const f32x4& a, const f32x4& b) { u32x4 w; w.x = cvt_pk_bf16(a[0], a[1]); w.y = cvt_pk_bf16(a[2], a[3]); w.z = cvt_pk_bf16(b[0], b[1]); w.w = cvt_pk_bf16(b[2], b[3]); return w; }
; __device__ __forceinline__ float sum4sq(const f32x4& a) { return (a[0] * a[0] + a[1] * a[1]) + (a[2] * a[2] + a[3] * a[3]); }
;     __device__ __forceinline__ void operator()(const AccT& acc, const Unit& u, int wr, int wc, int fr, int fq, const LAS f32x2* tab) const {
;     ...
;         for (int ai = 0; ai < 2; ++ai) {
;             u32x4 xwv[4][2];
; _Pragma("unroll")
;             for (int m = 0; m < 4; ++m)
; _Pragma("unroll")
;                 for (int bj = 0; bj < 2; ++bj) xwv[m][bj] = *(const GAS u32x4*)(xag + (size_t)(u.pm * 256 + ai * 128 + wr * 64 + m * 16 + fr) * 1024 + u.pn * 256 + bj * 128 + wc * 32 + fq * 8);
;             asm volatile("" ::: "memory");
; _Pragma("unroll")
;             for (int m = 0; m < 4; ++m) { const int rl = ai * 128 + wr * 64 + m * 16 + fr; const int row = u.pm * 256 + rl; const float rf = tab[rl].y; float s = 0.f;
; _Pragma("unroll")
;                 for (int bj = 0; bj < 2; ++bj) { const size_t off = (size_t)row * 1024 + u.pn * 256 + bj * 128 + wc * 32 + fq * 8; f32x4 b0, b1;
;                     { const u32x4 w = xwv[m][bj]; b0 = (f32x4){bflo(w.x), bfhi(w.x), bflo(w.y), bfhi(w.y)}; b1 = (f32x4){bflo(w.z), bfhi(w.z), bflo(w.w), bfhi(w.w)}; }
;                     const f32x4 v0 = b0 + acc[ai][bj][m][0] * rf, v1 = b1 + acc[ai][bj][m][1] * rf; s += sum4sq(v0) + sum4sq(v1);
;                     *(u32x4*)(xb + off) = pack8(v0, v1); }
;                 s = red_fq(s); if (fq == 0) ssx1[(size_t)row * 16 + u.pn * 4 + wc] = s; }
.LBB0_1633:
	s_or_b64 exec, exec, s[40:41]
	ds_read_b64 v[84:85], v130 offset:384
	v_lshlrev_b32_e32 v88, 16, v146
	v_and_b32_e32 v89, 0xffff0000, v146
	v_lshlrev_b32_e32 v90, 16, v147
	v_and_b32_e32 v91, 0xffff0000, v147
	v_lshlrev_b32_e32 v92, 16, v148
	v_and_b32_e32 v93, 0xffff0000, v148
	v_lshlrev_b32_e32 v94, 16, v149
	v_and_b32_e32 v95, 0xffff0000, v149
	s_waitcnt lgkmcnt(0)
	v_pk_fma_f32 v[82:83], v[82:83], v[84:85], v[90:91] op_sel:[0,1,0]
	v_pk_fma_f32 v[80:81], v[80:81], v[84:85], v[88:89] op_sel:[0,1,0]
	v_pk_fma_f32 v[88:89], v[78:79], v[84:85], v[94:95] op_sel:[0,1,0]
	v_pk_fma_f32 v[78:79], v[76:77], v[84:85], v[92:93] op_sel:[0,1,0]
	v_mul_f32_e32 v76, v81, v81
	v_mul_f32_e32 v77, v83, v83
	v_fmac_f32_e32 v76, v80, v80
	v_fmac_f32_e32 v77, v82, v82
	v_add_f32_e32 v76, v76, v77
	v_mul_f32_e32 v77, v79, v79
	v_mul_f32_e32 v90, v89, v89
	v_fmac_f32_e32 v77, v78, v78
	v_fmac_f32_e32 v90, v88, v88
	v_add_f32_e32 v77, v77, v90
	v_lshl_add_u64 v[86:87], v[132:133], 0, v[176:177]
	v_add_f32_e32 v90, v76, v77
	v_cvt_pk_bf16_f32 v76, v80, v81
	v_cvt_pk_bf16_f32 v77, v82, v83
	v_cvt_pk_bf16_f32 v78, v78, v79
	v_cvt_pk_bf16_f32 v79, v88, v89
	ds_bpermute_b32 v216, v220, v76
	ds_bpermute_b32 v217, v220, v77
	ds_bpermute_b32 v218, v220, v78
	ds_bpermute_b32 v219, v220, v79
	ds_bpermute_b32 v212, v220, v86
	ds_bpermute_b32 v213, v220, v87
	s_waitcnt lgkmcnt(0)
	global_store_dwordx4 v[212:213], v[216:219], off
	v_lshlrev_b32_e32 v80, 16, v144
	v_and_b32_e32 v81, 0xffff0000, v144
	v_lshlrev_b32_e32 v76, 16, v142
	v_and_b32_e32 v77, 0xffff0000, v142
	v_lshlrev_b32_e32 v78, 16, v143
	v_and_b32_e32 v79, 0xffff0000, v143
	v_lshlrev_b32_e32 v82, 16, v145
	v_and_b32_e32 v83, 0xffff0000, v145
	v_pk_fma_f32 v[74:75], v[74:75], v[84:85], v[78:79] op_sel:[0,1,0]
	v_pk_fma_f32 v[72:73], v[72:73], v[84:85], v[76:77] op_sel:[0,1,0]
	v_pk_fma_f32 v[76:77], v[70:71], v[84:85], v[82:83] op_sel:[0,1,0]
	v_pk_fma_f32 v[70:71], v[68:69], v[84:85], v[80:81] op_sel:[0,1,0]
	v_mul_f32_e32 v68, v73, v73
	v_mul_f32_e32 v69, v75, v75
	v_fmac_f32_e32 v68, v72, v72
	v_fmac_f32_e32 v69, v74, v74
	v_add_f32_e32 v68, v68, v69
	v_mul_f32_e32 v69, v71, v71
	v_mul_f32_e32 v78, v77, v77
	v_fmac_f32_e32 v69, v70, v70
	v_fmac_f32_e32 v78, v76, v76
	v_add_f32_e32 v69, v69, v78
	v_add_f32_e32 v68, v68, v69
	v_add_f32_e32 v78, v90, v68
	v_cvt_pk_bf16_f32 v68, v72, v73
	v_cvt_pk_bf16_f32 v69, v74, v75
	v_cvt_pk_bf16_f32 v70, v70, v71
	v_cvt_pk_bf16_f32 v71, v76, v77
	ds_bpermute_b32 v228, v220, v68
	ds_bpermute_b32 v229, v220, v69
	ds_bpermute_b32 v230, v220, v70
	ds_bpermute_b32 v231, v220, v71
	s_waitcnt lgkmcnt(0)
	global_store_dwordx4 v[212:213], v[228:231], off offset:256
	s_nop 1
	v_mov_b32_e32 v68, v78
	s_nop 1
	v_permlane16_swap_b32_e32 v78, v68
	v_add_f32_e32 v68, v78, v68
	v_mov_b32_e32 v69, v68
	s_nop 1
	v_permlane32_swap_b32_e32 v68, v69
	s_and_saveexec_b64 s[40:41], vcc
	s_cbranch_execz .LBB0_1635
	v_lshlrev_b64 v[70:71], 6, v[172:173]
	v_lshl_add_u64 v[70:71], s[26:27], 0, v[70:71]
	v_add_f32_e32 v68, v68, v69
	global_store_dword v[70:71], v68, off
.LBB0_1635:
	s_or_b64 exec, exec, s[40:41]
	v_add_u32_e32 v106, 0x80, v170
	v_ashrrev_i32_e32 v107, 31, v106
	v_lshlrev_b64 v[110:111], 11, v[106:107]
	v_lshl_add_u64 v[68:69], v[168:169], 0, v[110:111]
	ds_bpermute_b32 v214, v220, v68
	ds_bpermute_b32 v215, v220, v69
	s_waitcnt lgkmcnt(0)
	global_load_dwordx4 v[112:115], v[214:215], off
	global_load_dwordx4 v[92:95], v[214:215], off offset:256
	v_add_u32_e32 v102, 0x90, v170
	v_ashrrev_i32_e32 v103, 31, v102
	v_add_u32_e32 v98, 0xa0, v170
	v_lshlrev_b64 v[108:109], 11, v[102:103]
	v_ashrrev_i32_e32 v99, 31, v98
	v_add_u32_e32 v96, 0xb0, v170
	v_lshl_add_u64 v[68:69], v[168:169], 0, v[108:109]
	v_lshlrev_b64 v[104:105], 11, v[98:99]
	v_ashrrev_i32_e32 v97, 31, v96
	ds_bpermute_b32 v214, v220, v68
	ds_bpermute_b32 v215, v220, v69
	s_waitcnt lgkmcnt(0)
	global_load_dwordx4 v[88:91], v[214:215], off
	global_load_dwordx4 v[84:87], v[214:215], off offset:256
	v_lshl_add_u64 v[68:69], v[168:169], 0, v[104:105]
	v_lshlrev_b64 v[100:101], 11, v[96:97]
	ds_bpermute_b32 v214, v220, v68
	ds_bpermute_b32 v215, v220, v69
	s_waitcnt lgkmcnt(0)
	global_load_dwordx4 v[80:83], v[214:215], off
	global_load_dwordx4 v[76:79], v[214:215], off offset:256
	v_lshl_add_u64 v[68:69], v[168:169], 0, v[100:101]
	ds_bpermute_b32 v214, v220, v68
	ds_bpermute_b32 v215, v220, v69
	s_waitcnt lgkmcnt(0)
	global_load_dwordx4 v[72:75], v[214:215], off
	s_nop 0
	ds_bpermute_b32 v214, v220, v68
	ds_bpermute_b32 v215, v220, v69
	s_waitcnt lgkmcnt(0)
	global_load_dwordx4 v[68:71], v[214:215], off offset:256
	ds_read_b64 v[116:117], v130 offset:1024
	v_lshl_add_u64 v[110:111], v[132:133], 0, v[110:111]
	s_waitcnt vmcnt(7)
	ds_bpermute_b32 v112, v220, v112
	ds_bpermute_b32 v113, v220, v113
	ds_bpermute_b32 v114, v220, v114
	ds_bpermute_b32 v115, v220, v115
	s_waitcnt lgkmcnt(0)
	v_lshlrev_b32_e32 v118, 16, v112
	v_and_b32_e32 v119, 0xffff0000, v112
	v_lshlrev_b32_e32 v112, 16, v113
	v_and_b32_e32 v113, 0xffff0000, v113
	s_waitcnt lgkmcnt(0)
	v_pk_fma_f32 v[62:63], v[62:63], v[116:117], v[112:113] op_sel:[0,1,0]
	v_pk_fma_f32 v[60:61], v[60:61], v[116:117], v[118:119] op_sel:[0,1,0]
	v_lshlrev_b32_e32 v120, 16, v114
	v_and_b32_e32 v121, 0xffff0000, v114
	v_lshlrev_b32_e32 v114, 16, v115
	v_and_b32_e32 v115, 0xffff0000, v115
	v_mul_f32_e32 v112, v61, v61
	v_mul_f32_e32 v113, v63, v63
	v_pk_fma_f32 v[66:67], v[66:67], v[116:117], v[114:115] op_sel:[0,1,0]
	v_pk_fma_f32 v[64:65], v[64:65], v[116:117], v[120:121] op_sel:[0,1,0]
	v_fmac_f32_e32 v112, v60, v60
	v_fmac_f32_e32 v113, v62, v62
	v_cvt_pk_bf16_f32 v60, v60, v61
	v_cvt_pk_bf16_f32 v61, v62, v63
	v_cvt_pk_bf16_f32 v62, v64, v65
	v_cvt_pk_bf16_f32 v63, v66, v67
	v_add_f32_e32 v112, v112, v113
	v_mul_f32_e32 v113, v65, v65
	v_mul_f32_e32 v114, v67, v67
	ds_bpermute_b32 v216, v220, v60
	ds_bpermute_b32 v217, v220, v61
	ds_bpermute_b32 v218, v220, v62
	ds_bpermute_b32 v219, v220, v63
	ds_bpermute_b32 v212, v220, v110
	ds_bpermute_b32 v213, v220, v111
	s_waitcnt lgkmcnt(0)
; __device__ __forceinline__ float bflo(unsigned w) { return __uint_as_float(w << 16); }
; __device__ __forceinline__ float bfhi(unsigned w) { return __uint_as_float(w & 0xffff0000u); }
; __device__ __forceinline__ u32x4 pack8(const f32x4& a, const f32x4& b) { u32x4 w; w.x = cvt_pk_bf16(a[0], a[1]); w.y = cvt_pk_bf16(a[2], a[3]); w.z = cvt_pk_bf16(b[0], b[1]); w.w = cvt_pk_bf16(b[2], b[3]); return w; }
; __device__ __forceinline__ float sum4sq(const f32x4& a) { return (a[0] * a[0] + a[1] * a[1]) + (a[2] * a[2] + a[3] * a[3]); }
;     __device__ __forceinline__ void operator()(const AccT& acc, const Unit& u, int wr, int wc, int fr, int fq, const LAS f32x2* tab) const {
;     ...
;             for (int m = 0; m < 4; ++m) { const int rl = ai * 128 + wr * 64 + m * 16 + fr; const int row = u.pm * 256 + rl; const float rf = tab[rl].y; float s = 0.f;
; _Pragma("unroll")
;                 for (int bj = 0; bj < 2; ++bj) { const size_t off = (size_t)row * 1024 + u.pn * 256 + bj * 128 + wc * 32 + fq * 8; f32x4 b0, b1;
;                     { const u32x4 w = xwv[m][bj]; b0 = (f32x4){bflo(w.x), bfhi(w.x), bflo(w.y), bfhi(w.y)}; b1 = (f32x4){bflo(w.z), bfhi(w.z), bflo(w.w), bfhi(w.w)}; }
;                     const f32x4 v0 = b0 + acc[ai][bj][m][0] * rf, v1 = b1 + acc[ai][bj][m][1] * rf; s += sum4sq(v0) + sum4sq(v1);
;                     *(u32x4*)(xb + off) = pack8(v0, v1); }
;                 s = red_fq(s); if (fq == 0) ssx1[(size_t)row * 16 + u.pn * 4 + wc] = s; }
	global_store_dwordx4 v[212:213], v[216:219], off
	v_fmac_f32_e32 v113, v64, v64
	v_fmac_f32_e32 v114, v66, v66
	s_waitcnt vmcnt(7)
	ds_bpermute_b32 v92, v220, v92
	ds_bpermute_b32 v93, v220, v93
	ds_bpermute_b32 v94, v220, v94
	ds_bpermute_b32 v95, v220, v95
	s_waitcnt lgkmcnt(0)
	v_lshlrev_b32_e32 v60, 16, v92
	v_and_b32_e32 v61, 0xffff0000, v92
	v_lshlrev_b32_e32 v62, 16, v93
	v_and_b32_e32 v63, 0xffff0000, v93
	v_lshlrev_b32_e32 v64, 16, v94
	v_and_b32_e32 v65, 0xffff0000, v94
	v_lshlrev_b32_e32 v66, 16, v95
	v_and_b32_e32 v67, 0xffff0000, v95
	v_pk_fma_f32 v[58:59], v[58:59], v[116:117], v[62:63] op_sel:[0,1,0]
	v_pk_fma_f32 v[56:57], v[56:57], v[116:117], v[60:61] op_sel:[0,1,0]
	v_pk_fma_f32 v[60:61], v[54:55], v[116:117], v[66:67] op_sel:[0,1,0]
	v_pk_fma_f32 v[54:55], v[52:53], v[116:117], v[64:65] op_sel:[0,1,0]
	v_mul_f32_e32 v52, v57, v57
	v_mul_f32_e32 v53, v59, v59
	v_fmac_f32_e32 v52, v56, v56
	v_fmac_f32_e32 v53, v58, v58
	v_add_f32_e32 v52, v52, v53
	v_mul_f32_e32 v53, v55, v55
	v_mul_f32_e32 v62, v61, v61
	v_fmac_f32_e32 v53, v54, v54
	v_fmac_f32_e32 v62, v60, v60
	v_add_f32_e32 v113, v113, v114
	v_add_f32_e32 v53, v53, v62
	v_add_f32_e32 v112, v112, v113
	v_add_f32_e32 v52, v52, v53
	v_add_f32_e32 v62, v112, v52
	v_cvt_pk_bf16_f32 v52, v56, v57
	v_cvt_pk_bf16_f32 v53, v58, v59
	v_cvt_pk_bf16_f32 v54, v54, v55
	v_cvt_pk_bf16_f32 v55, v60, v61
	ds_bpermute_b32 v228, v220, v52
	ds_bpermute_b32 v229, v220, v53
	ds_bpermute_b32 v230, v220, v54
	ds_bpermute_b32 v231, v220, v55
	s_waitcnt lgkmcnt(0)
	global_store_dwordx4 v[212:213], v[228:231], off offset:256
	s_nop 1
	v_mov_b32_e32 v52, v62
	s_nop 1
	v_permlane16_swap_b32_e32 v62, v52
	v_add_f32_e32 v52, v62, v52
	v_mov_b32_e32 v53, v52
	s_nop 1
	v_permlane32_swap_b32_e32 v52, v53
	s_and_saveexec_b64 s[40:41], vcc
	s_cbranch_execz .LBB0_1637
	v_lshlrev_b64 v[54:55], 6, v[106:107]
	v_lshl_add_u64 v[54:55], s[26:27], 0, v[54:55]
	v_add_f32_e32 v52, v52, v53
	global_store_dword v[54:55], v52, off
.LBB0_1637:
	s_or_b64 exec, exec, s[40:41]
	ds_read_b64 v[52:53], v130 offset:1152
	s_waitcnt vmcnt(7)
	ds_bpermute_b32 v88, v220, v88
	ds_bpermute_b32 v89, v220, v89
	ds_bpermute_b32 v90, v220, v90
	ds_bpermute_b32 v91, v220, v91
	s_waitcnt lgkmcnt(0)
	v_lshlrev_b32_e32 v56, 16, v88
	v_and_b32_e32 v57, 0xffff0000, v88
	v_lshlrev_b32_e32 v58, 16, v89
	v_and_b32_e32 v59, 0xffff0000, v89
	v_lshlrev_b32_e32 v60, 16, v90
	v_and_b32_e32 v61, 0xffff0000, v90
	v_lshlrev_b32_e32 v62, 16, v91
	v_and_b32_e32 v63, 0xffff0000, v91
	s_waitcnt lgkmcnt(0)
	v_pk_fma_f32 v[50:51], v[50:51], v[52:53], v[58:59] op_sel:[0,1,0]
	v_pk_fma_f32 v[48:49], v[48:49], v[52:53], v[56:57] op_sel:[0,1,0]
	v_pk_fma_f32 v[56:57], v[46:47], v[52:53], v[62:63] op_sel:[0,1,0]
	v_pk_fma_f32 v[46:47], v[44:45], v[52:53], v[60:61] op_sel:[0,1,0]
	v_mul_f32_e32 v44, v49, v49
	v_mul_f32_e32 v45, v51, v51
	v_fmac_f32_e32 v44, v48, v48
	v_fmac_f32_e32 v45, v50, v50
	v_add_f32_e32 v44, v44, v45
	v_mul_f32_e32 v45, v47, v47
	v_mul_f32_e32 v58, v57, v57
	v_fmac_f32_e32 v45, v46, v46
	v_fmac_f32_e32 v58, v56, v56
	v_add_f32_e32 v45, v45, v58
	v_lshl_add_u64 v[54:55], v[132:133], 0, v[108:109]
	v_add_f32_e32 v58, v44, v45
	v_cvt_pk_bf16_f32 v44, v48, v49
	v_cvt_pk_bf16_f32 v45, v50, v51
	v_cvt_pk_bf16_f32 v46, v46, v47
	v_cvt_pk_bf16_f32 v47, v56, v57
	ds_bpermute_b32 v216, v220, v44
	ds_bpermute_b32 v217, v220, v45
	ds_bpermute_b32 v218, v220, v46
	ds_bpermute_b32 v219, v220, v47
	ds_bpermute_b32 v212, v220, v54
	ds_bpermute_b32 v213, v220, v55
	s_waitcnt lgkmcnt(0)
	global_store_dwordx4 v[212:213], v[216:219], off
	s_waitcnt vmcnt(7)
	ds_bpermute_b32 v84, v220, v84
	ds_bpermute_b32 v85, v220, v85
	ds_bpermute_b32 v86, v220, v86
	ds_bpermute_b32 v87, v220, v87
	s_waitcnt lgkmcnt(0)
	v_lshlrev_b32_e32 v48, 16, v86
	v_and_b32_e32 v49, 0xffff0000, v86
	v_lshlrev_b32_e32 v44, 16, v84
	v_and_b32_e32 v45, 0xffff0000, v84
	v_lshlrev_b32_e32 v46, 16, v85
	v_and_b32_e32 v47, 0xffff0000, v85
	v_lshlrev_b32_e32 v50, 16, v87
	v_and_b32_e32 v51, 0xffff0000, v87
	v_pk_fma_f32 v[42:43], v[42:43], v[52:53], v[46:47] op_sel:[0,1,0]
	v_pk_fma_f32 v[40:41], v[40:41], v[52:53], v[44:45] op_sel:[0,1,0]
	v_pk_fma_f32 v[44:45], v[38:39], v[52:53], v[50:51] op_sel:[0,1,0]
	v_pk_fma_f32 v[38:39], v[36:37], v[52:53], v[48:49] op_sel:[0,1,0]
	v_mul_f32_e32 v36, v41, v41
	v_mul_f32_e32 v37, v43, v43
	v_fmac_f32_e32 v36, v40, v40
	v_fmac_f32_e32 v37, v42, v42
	v_add_f32_e32 v36, v36, v37
	v_mul_f32_e32 v37, v39, v39
	v_mul_f32_e32 v46, v45, v45
	v_fmac_f32_e32 v37, v38, v38
	v_fmac_f32_e32 v46, v44, v44
	v_add_f32_e32 v37, v37, v46
	v_add_f32_e32 v36, v36, v37
	v_add_f32_e32 v46, v58, v36
	v_cvt_pk_bf16_f32 v36, v40, v41
	v_cvt_pk_bf16_f32 v37, v42, v43
	v_cvt_pk_bf16_f32 v38, v38, v39
	v_cvt_pk_bf16_f32 v39, v44, v45
	ds_bpermute_b32 v228, v220, v36
	ds_bpermute_b32 v229, v220, v37
	ds_bpermute_b32 v230, v220, v38
	ds_bpermute_b32 v231, v220, v39
	s_waitcnt lgkmcnt(0)
	global_store_dwordx4 v[212:213], v[228:231], off offset:256
	s_nop 1
	v_mov_b32_e32 v36, v46
	s_nop 1
	v_permlane16_swap_b32_e32 v46, v36
	v_add_f32_e32 v36, v46, v36
	v_mov_b32_e32 v37, v36
	s_nop 1
	v_permlane32_swap_b32_e32 v36, v37
	s_and_saveexec_b64 s[40:41], vcc
	s_cbranch_execz .LBB0_1639
	v_lshlrev_b64 v[38:39], 6, v[102:103]
	v_lshl_add_u64 v[38:39], s[26:27], 0, v[38:39]
	v_add_f32_e32 v36, v36, v37
	global_store_dword v[38:39], v36, off
; __device__ __forceinline__ float bflo(unsigned w) { return __uint_as_float(w << 16); }
; __device__ __forceinline__ float bfhi(unsigned w) { return __uint_as_float(w & 0xffff0000u); }
; __device__ __forceinline__ u32x4 pack8(const f32x4& a, const f32x4& b) { u32x4 w; w.x = cvt_pk_bf16(a[0], a[1]); w.y = cvt_pk_bf16(a[2], a[3]); w.z = cvt_pk_bf16(b[0], b[1]); w.w = cvt_pk_bf16(b[2], b[3]); return w; }
; __device__ __forceinline__ float sum4sq(const f32x4& a) { return (a[0] * a[0] + a[1] * a[1]) + (a[2] * a[2] + a[3] * a[3]); }
;     __device__ __forceinline__ void operator()(const AccT& acc, const Unit& u, int wr, int wc, int fr, int fq, const LAS f32x2* tab) const {
;     ...
;             for (int m = 0; m < 4; ++m) { const int rl = ai * 128 + wr * 64 + m * 16 + fr; const int row = u.pm * 256 + rl; const float rf = tab[rl].y; float s = 0.f;
; _Pragma("unroll")
;                 for (int bj = 0; bj < 2; ++bj) { const size_t off = (size_t)row * 1024 + u.pn * 256 + bj * 128 + wc * 32 + fq * 8; f32x4 b0, b1;
;                     { const u32x4 w = xwv[m][bj]; b0 = (f32x4){bflo(w.x), bfhi(w.x), bflo(w.y), bfhi(w.y)}; b1 = (f32x4){bflo(w.z), bfhi(w.z), bflo(w.w), bfhi(w.w)}; }
;                     const f32x4 v0 = b0 + acc[ai][bj][m][0] * rf, v1 = b1 + acc[ai][bj][m][1] * rf; s += sum4sq(v0) + sum4sq(v1);
;                     *(u32x4*)(xb + off) = pack8(v0, v1); }
;                 s = red_fq(s); if (fq == 0) ssx1[(size_t)row * 16 + u.pn * 4 + wc] = s; }
.LBB0_1639:
	s_or_b64 exec, exec, s[40:41]
	ds_read_b64 v[36:37], v130 offset:1280
	s_waitcnt vmcnt(7)
	ds_bpermute_b32 v80, v220, v80
	ds_bpermute_b32 v81, v220, v81
	ds_bpermute_b32 v82, v220, v82
	ds_bpermute_b32 v83, v220, v83
	s_waitcnt lgkmcnt(0)
	v_lshlrev_b32_e32 v40, 16, v80
	v_and_b32_e32 v41, 0xffff0000, v80
	v_lshlrev_b32_e32 v42, 16, v81
	v_and_b32_e32 v43, 0xffff0000, v81
	v_lshlrev_b32_e32 v44, 16, v82
	v_and_b32_e32 v45, 0xffff0000, v82
	v_lshlrev_b32_e32 v46, 16, v83
	v_and_b32_e32 v47, 0xffff0000, v83
	s_waitcnt lgkmcnt(0)
	v_pk_fma_f32 v[34:35], v[34:35], v[36:37], v[42:43] op_sel:[0,1,0]
	v_pk_fma_f32 v[32:33], v[32:33], v[36:37], v[40:41] op_sel:[0,1,0]
	v_pk_fma_f32 v[40:41], v[30:31], v[36:37], v[46:47] op_sel:[0,1,0]
	v_pk_fma_f32 v[30:31], v[28:29], v[36:37], v[44:45] op_sel:[0,1,0]
	v_mul_f32_e32 v28, v33, v33
	v_mul_f32_e32 v29, v35, v35
	v_fmac_f32_e32 v28, v32, v32
	v_fmac_f32_e32 v29, v34, v34
	v_add_f32_e32 v28, v28, v29
	v_mul_f32_e32 v29, v31, v31
	v_mul_f32_e32 v42, v41, v41
	v_fmac_f32_e32 v29, v30, v30
	v_fmac_f32_e32 v42, v40, v40
	v_add_f32_e32 v29, v29, v42
	v_lshl_add_u64 v[38:39], v[132:133], 0, v[104:105]
	v_add_f32_e32 v42, v28, v29
	v_cvt_pk_bf16_f32 v28, v32, v33
	v_cvt_pk_bf16_f32 v29, v34, v35
	v_cvt_pk_bf16_f32 v30, v30, v31
	v_cvt_pk_bf16_f32 v31, v40, v41
	ds_bpermute_b32 v216, v220, v28
	ds_bpermute_b32 v217, v220, v29
	ds_bpermute_b32 v218, v220, v30
	ds_bpermute_b32 v219, v220, v31
	ds_bpermute_b32 v212, v220, v38
	ds_bpermute_b32 v213, v220, v39
	s_waitcnt lgkmcnt(0)
	global_store_dwordx4 v[212:213], v[216:219], off
	s_waitcnt vmcnt(7)
	ds_bpermute_b32 v76, v220, v76
	ds_bpermute_b32 v77, v220, v77
	ds_bpermute_b32 v78, v220, v78
	ds_bpermute_b32 v79, v220, v79
	s_waitcnt lgkmcnt(0)
	v_lshlrev_b32_e32 v32, 16, v78
	v_and_b32_e32 v33, 0xffff0000, v78
	v_lshlrev_b32_e32 v28, 16, v76
	v_and_b32_e32 v29, 0xffff0000, v76
	v_lshlrev_b32_e32 v30, 16, v77
	v_and_b32_e32 v31, 0xffff0000, v77
	v_lshlrev_b32_e32 v34, 16, v79
	v_and_b32_e32 v35, 0xffff0000, v79
	v_pk_fma_f32 v[26:27], v[26:27], v[36:37], v[30:31] op_sel:[0,1,0]
	v_pk_fma_f32 v[24:25], v[24:25], v[36:37], v[28:29] op_sel:[0,1,0]
	v_pk_fma_f32 v[28:29], v[22:23], v[36:37], v[34:35] op_sel:[0,1,0]
	v_pk_fma_f32 v[22:23], v[20:21], v[36:37], v[32:33] op_sel:[0,1,0]
	v_mul_f32_e32 v20, v25, v25
	v_mul_f32_e32 v21, v27, v27
	v_fmac_f32_e32 v20, v24, v24
	v_fmac_f32_e32 v21, v26, v26
	v_add_f32_e32 v20, v20, v21
	v_mul_f32_e32 v21, v23, v23
	v_mul_f32_e32 v30, v29, v29
	v_fmac_f32_e32 v21, v22, v22
	v_fmac_f32_e32 v30, v28, v28
	v_add_f32_e32 v21, v21, v30
	v_add_f32_e32 v20, v20, v21
	v_add_f32_e32 v30, v42, v20
	v_cvt_pk_bf16_f32 v20, v24, v25
	v_cvt_pk_bf16_f32 v21, v26, v27
	v_cvt_pk_bf16_f32 v22, v22, v23
	v_cvt_pk_bf16_f32 v23, v28, v29
	ds_bpermute_b32 v228, v220, v20
	ds_bpermute_b32 v229, v220, v21
	ds_bpermute_b32 v230, v220, v22
	ds_bpermute_b32 v231, v220, v23
	s_waitcnt lgkmcnt(0)
	global_store_dwordx4 v[212:213], v[228:231], off offset:256
	s_nop 1
	v_mov_b32_e32 v20, v30
	s_nop 1
	v_permlane16_swap_b32_e32 v30, v20
	v_add_f32_e32 v20, v30, v20
	v_mov_b32_e32 v21, v20
	s_nop 1
	v_permlane32_swap_b32_e32 v20, v21
	s_and_saveexec_b64 s[40:41], vcc
	s_cbranch_execz .LBB0_1641
	v_lshlrev_b64 v[22:23], 6, v[98:99]
	v_lshl_add_u64 v[22:23], s[26:27], 0, v[22:23]
	v_add_f32_e32 v20, v20, v21
	global_store_dword v[22:23], v20, off
.LBB0_1641:
	s_or_b64 exec, exec, s[40:41]
	ds_read_b64 v[20:21], v130 offset:1408
	s_waitcnt vmcnt(7)
	ds_bpermute_b32 v72, v220, v72
	ds_bpermute_b32 v73, v220, v73
	ds_bpermute_b32 v74, v220, v74
	ds_bpermute_b32 v75, v220, v75
	s_waitcnt lgkmcnt(0)
	v_lshlrev_b32_e32 v24, 16, v72
	v_and_b32_e32 v25, 0xffff0000, v72
	v_lshlrev_b32_e32 v26, 16, v73
	v_and_b32_e32 v27, 0xffff0000, v73
	v_lshlrev_b32_e32 v28, 16, v74
	v_and_b32_e32 v29, 0xffff0000, v74
	v_lshlrev_b32_e32 v30, 16, v75
	v_and_b32_e32 v31, 0xffff0000, v75
	s_waitcnt lgkmcnt(0)
	v_pk_fma_f32 v[18:19], v[18:19], v[20:21], v[26:27] op_sel:[0,1,0]
	v_pk_fma_f32 v[16:17], v[16:17], v[20:21], v[24:25] op_sel:[0,1,0]
	v_pk_fma_f32 v[24:25], v[14:15], v[20:21], v[30:31] op_sel:[0,1,0]
	v_pk_fma_f32 v[14:15], v[12:13], v[20:21], v[28:29] op_sel:[0,1,0]
	v_mul_f32_e32 v12, v17, v17
	v_mul_f32_e32 v13, v19, v19
	v_fmac_f32_e32 v12, v16, v16
	v_fmac_f32_e32 v13, v18, v18
	v_add_f32_e32 v12, v12, v13
	v_mul_f32_e32 v13, v15, v15
	v_mul_f32_e32 v26, v25, v25
	v_fmac_f32_e32 v13, v14, v14
	v_fmac_f32_e32 v26, v24, v24
	v_add_f32_e32 v13, v13, v26
	v_lshl_add_u64 v[22:23], v[132:133], 0, v[100:101]
	v_add_f32_e32 v26, v12, v13
	v_cvt_pk_bf16_f32 v12, v16, v17
	v_cvt_pk_bf16_f32 v13, v18, v19
	v_cvt_pk_bf16_f32 v14, v14, v15
	v_cvt_pk_bf16_f32 v15, v24, v25
	ds_bpermute_b32 v216, v220, v12
	ds_bpermute_b32 v217, v220, v13
	ds_bpermute_b32 v218, v220, v14
	ds_bpermute_b32 v219, v220, v15
	ds_bpermute_b32 v212, v220, v22
	ds_bpermute_b32 v213, v220, v23
	s_waitcnt lgkmcnt(0)
	global_store_dwordx4 v[212:213], v[216:219], off
	s_waitcnt vmcnt(7)
	ds_bpermute_b32 v68, v220, v68
	ds_bpermute_b32 v69, v220, v69
	ds_bpermute_b32 v70, v220, v70
	ds_bpermute_b32 v71, v220, v71
	s_waitcnt lgkmcnt(0)
	v_lshlrev_b32_e32 v16, 16, v70
	v_and_b32_e32 v17, 0xffff0000, v70
	v_lshlrev_b32_e32 v12, 16, v68
	v_and_b32_e32 v13, 0xffff0000, v68
	v_lshlrev_b32_e32 v14, 16, v69
	v_and_b32_e32 v15, 0xffff0000, v69
	v_lshlrev_b32_e32 v18, 16, v71
	v_and_b32_e32 v19, 0xffff0000, v71
	v_pk_fma_f32 v[10:11], v[10:11], v[20:21], v[14:15] op_sel:[0,1,0]
	v_pk_fma_f32 v[8:9], v[8:9], v[20:21], v[12:13] op_sel:[0,1,0]
	v_pk_fma_f32 v[12:13], v[6:7], v[20:21], v[18:19] op_sel:[0,1,0]
	v_pk_fma_f32 v[6:7], v[4:5], v[20:21], v[16:17] op_sel:[0,1,0]
	v_mul_f32_e32 v4, v9, v9
	v_mul_f32_e32 v5, v11, v11
	v_fmac_f32_e32 v4, v8, v8
	v_fmac_f32_e32 v5, v10, v10
	v_add_f32_e32 v4, v4, v5
	v_mul_f32_e32 v5, v7, v7
	v_mul_f32_e32 v14, v13, v13
	v_fmac_f32_e32 v5, v6, v6
	v_fmac_f32_e32 v14, v12, v12
	v_add_f32_e32 v5, v5, v14
	v_add_f32_e32 v4, v4, v5
	v_add_f32_e32 v14, v26, v4
	v_cvt_pk_bf16_f32 v4, v8, v9
	v_cvt_pk_bf16_f32 v5, v10, v11
	v_cvt_pk_bf16_f32 v6, v6, v7
	v_cvt_pk_bf16_f32 v7, v12, v13
	ds_bpermute_b32 v228, v220, v4
	ds_bpermute_b32 v229, v220, v5
	ds_bpermute_b32 v230, v220, v6
	ds_bpermute_b32 v231, v220, v7
	s_waitcnt lgkmcnt(0)
	global_store_dwordx4 v[212:213], v[228:231], off offset:256
	s_nop 1
	v_mov_b32_e32 v4, v14
	s_nop 1
	v_permlane16_swap_b32_e32 v14, v4
	v_add_f32_e32 v4, v14, v4
	v_mov_b32_e32 v5, v4
	s_nop 1
	v_permlane32_swap_b32_e32 v4, v5
	s_and_saveexec_b64 s[40:41], vcc
	s_cbranch_execz .LBB0_1643
	v_lshlrev_b64 v[6:7], 6, v[96:97]
	v_lshl_add_u64 v[6:7], s[26:27], 0, v[6:7]
	v_add_f32_e32 v4, v4, v5
	global_store_dword v[6:7], v4, off
